# v54 plus P10 token-1 load wait relaxed from vmcnt(0) to vmcnt(3) (younger stores no longer waited for)
# baseline (speedup 1.0000x reference)
.LBB0_1064:
	s_waitcnt vmcnt(8)
	v_cvt_pk_f32_fp8_e32 v[74:75], v52
	s_waitcnt vmcnt(3)
	v_lshlrev_b32_e32 v64, 16, v60
	v_and_b32_e32 v65, 0xffff0000, v60
	v_cvt_pk_f32_fp8_sdwa v[72:73], v52 src0_sel:WORD_1
	v_pk_mul_f32 v[74:75], v[96:97], v[74:75] op_sel_hi:[0,1]
	v_cvt_pk_f32_fp8_sdwa v[76:77], v53 src0_sel:WORD_1
	v_cvt_pk_f32_fp8_e32 v[52:53], v53
	v_pk_fma_f32 v[64:65], v[64:65], s[92:93], v[74:75] op_sel_hi:[1,0,1]
	v_cvt_pk_f32_fp8_sdwa v[74:75], v54 src0_sel:WORD_1
	v_lshlrev_b32_e32 v60, 16, v61
	v_and_b32_e32 v61, 0xffff0000, v61
	v_lshlrev_b32_e32 v66, 16, v62
	v_and_b32_e32 v67, 0xffff0000, v62
	v_pk_mul_f32 v[72:73], v[96:97], v[72:73] op_sel_hi:[0,1]
	v_pk_mul_f32 v[52:53], v[96:97], v[52:53] op_sel_hi:[0,1]
	v_pk_fma_f32 v[60:61], v[60:61], s[92:93], v[72:73] op_sel_hi:[1,0,1]
	v_pk_mul_f32 v[72:73], v[96:97], v[76:77] op_sel_hi:[0,1]
	v_cvt_pk_f32_fp8_e32 v[76:77], v54
	v_pk_fma_f32 v[52:53], v[66:67], s[92:93], v[52:53] op_sel_hi:[1,0,1]
	v_pk_mul_f32 v[66:67], v[96:97], v[74:75] op_sel_hi:[0,1]
	v_cvt_pk_f32_fp8_sdwa v[74:75], v55 src0_sel:WORD_1
	v_cvt_pk_f32_fp8_e32 v[54:55], v55
	v_lshlrev_b32_e32 v62, 16, v63
	v_and_b32_e32 v63, 0xffff0000, v63
	v_lshlrev_b32_e32 v68, 16, v56
	v_and_b32_e32 v69, 0xffff0000, v56
	v_lshlrev_b32_e32 v56, 16, v57
	v_and_b32_e32 v57, 0xffff0000, v57
	v_lshlrev_b32_e32 v70, 16, v58
	v_and_b32_e32 v71, 0xffff0000, v58
	v_lshlrev_b32_e32 v58, 16, v59
	v_and_b32_e32 v59, 0xffff0000, v59
	v_pk_fma_f32 v[62:63], v[62:63], s[92:93], v[72:73] op_sel_hi:[1,0,1]
	v_pk_mul_f32 v[72:73], v[96:97], v[76:77] op_sel_hi:[0,1]
	v_pk_fma_f32 v[56:57], v[56:57], s[92:93], v[66:67] op_sel_hi:[1,0,1]
	v_pk_mul_f32 v[66:67], v[96:97], v[74:75] op_sel_hi:[0,1]
	v_pk_mul_f32 v[54:55], v[96:97], v[54:55] op_sel_hi:[0,1]
	v_pk_fma_f32 v[68:69], v[68:69], s[92:93], v[72:73] op_sel_hi:[1,0,1]
	v_pk_fma_f32 v[54:55], v[70:71], s[92:93], v[54:55] op_sel_hi:[1,0,1]
	v_pk_fma_f32 v[58:59], v[58:59], s[92:93], v[66:67] op_sel_hi:[1,0,1]
	v_cvt_pk_f32_fp8_sdwa v[66:67], v48 src0_sel:WORD_1
	v_cvt_pk_f32_fp8_e32 v[70:71], v48
	v_cvt_pk_f32_fp8_sdwa v[72:73], v49 src0_sel:WORD_1
	v_cvt_pk_f32_fp8_e32 v[48:49], v49
	v_pk_fma_f32 v[60:61], v[94:95], v[66:67], v[60:61] op_sel_hi:[0,1,1]
	v_pk_fma_f32 v[64:65], v[94:95], v[70:71], v[64:65] op_sel_hi:[0,1,1]
	v_cvt_pk_f32_fp8_e32 v[66:67], v50
	v_pk_fma_f32 v[48:49], v[94:95], v[48:49], v[52:53] op_sel_hi:[0,1,1]
	v_cvt_pk_f32_fp8_sdwa v[52:53], v50 src0_sel:WORD_1
	v_cvt_pk_f32_fp8_sdwa v[70:71], v51 src0_sel:WORD_1
	v_cvt_pk_f32_fp8_e32 v[50:51], v51
	v_pk_fma_f32 v[62:63], v[94:95], v[72:73], v[62:63] op_sel_hi:[0,1,1]
	v_pk_fma_f32 v[52:53], v[94:95], v[52:53], v[56:57] op_sel_hi:[0,1,1]
	v_pk_fma_f32 v[56:57], v[94:95], v[66:67], v[68:69] op_sel_hi:[0,1,1]
	v_pk_fma_f32 v[50:51], v[94:95], v[50:51], v[54:55] op_sel_hi:[0,1,1]
	v_cvt_pk_f32_fp8_e32 v[54:55], v44
	v_cvt_pk_f32_fp8_sdwa v[66:67], v44 src0_sel:WORD_1
	v_cvt_pk_f32_fp8_e32 v[68:69], v45
	v_cvt_pk_f32_fp8_sdwa v[44:45], v45 src0_sel:WORD_1
	v_pk_fma_f32 v[54:55], v[92:93], v[54:55], v[64:65] op_sel_hi:[0,1,1]
	v_pk_fma_f32 v[60:61], v[92:93], v[66:67], v[60:61] op_sel_hi:[0,1,1]
	v_cvt_pk_f32_fp8_sdwa v[64:65], v46 src0_sel:WORD_1
	v_pk_fma_f32 v[44:45], v[92:93], v[44:45], v[62:63] op_sel_hi:[0,1,1]
	v_cvt_pk_f32_fp8_e32 v[62:63], v46
	v_cvt_pk_f32_fp8_e32 v[66:67], v47
	v_cvt_pk_f32_fp8_sdwa v[46:47], v47 src0_sel:WORD_1
	v_pk_fma_f32 v[58:59], v[94:95], v[70:71], v[58:59] op_sel_hi:[0,1,1]
	v_pk_fma_f32 v[56:57], v[92:93], v[62:63], v[56:57] op_sel_hi:[0,1,1]
	v_pk_fma_f32 v[52:53], v[92:93], v[64:65], v[52:53] op_sel_hi:[0,1,1]
	v_pk_fma_f32 v[46:47], v[92:93], v[46:47], v[58:59] op_sel_hi:[0,1,1]
	v_cvt_pk_f32_fp8_sdwa v[58:59], v40 src0_sel:WORD_1
	v_cvt_pk_f32_fp8_e32 v[62:63], v40
	v_cvt_pk_f32_fp8_sdwa v[64:65], v41 src0_sel:WORD_1
	v_cvt_pk_f32_fp8_e32 v[40:41], v41
	v_pk_fma_f32 v[48:49], v[92:93], v[68:69], v[48:49] op_sel_hi:[0,1,1]
	s_waitcnt lgkmcnt(0)
	v_pk_fma_f32 v[58:59], v[2:3], v[58:59], v[60:61] op_sel_hi:[0,1,1]
	v_pk_fma_f32 v[54:55], v[2:3], v[62:63], v[54:55] op_sel_hi:[0,1,1]
	v_pk_fma_f32 v[48:49], v[2:3], v[40:41], v[48:49] op_sel_hi:[0,1,1]
	v_cvt_pk_f32_fp8_sdwa v[40:41], v42 src0_sel:WORD_1
	v_cvt_pk_f32_fp8_e32 v[60:61], v42
	v_cvt_pk_f32_fp8_sdwa v[62:63], v43 src0_sel:WORD_1
	v_cvt_pk_f32_fp8_e32 v[42:43], v43
	v_pk_fma_f32 v[50:51], v[92:93], v[66:67], v[50:51] op_sel_hi:[0,1,1]
	v_pk_fma_f32 v[44:45], v[2:3], v[64:65], v[44:45] op_sel_hi:[0,1,1]
	v_pk_fma_f32 v[52:53], v[2:3], v[40:41], v[52:53] op_sel_hi:[0,1,1]
	v_pk_fma_f32 v[56:57], v[2:3], v[60:61], v[56:57] op_sel_hi:[0,1,1]
	v_pk_fma_f32 v[60:61], v[2:3], v[62:63], v[46:47] op_sel_hi:[0,1,1]
	v_pk_fma_f32 v[62:63], v[2:3], v[42:43], v[50:51] op_sel_hi:[0,1,1]
	v_pk_mov_b32 v[40:41], v[54:55], v[58:59] op_sel:[1,0]
	v_mov_b32_e32 v42, v54
	v_mov_b32_e32 v43, v59
	v_pk_add_f32 v[40:41], v[40:41], v[42:43]
	v_pk_mov_b32 v[42:43], v[48:49], v[44:45] op_sel:[1,0]
	v_mov_b32_e32 v46, v48
	v_mov_b32_e32 v47, v45
	v_pk_add_f32 v[42:43], v[42:43], v[46:47]
	v_add_f32_e32 v2, v40, v41
	v_pk_add_f32 v[42:43], v[42:43], v[42:43] op_sel:[0,1] op_sel_hi:[1,0]
	v_add_f32_e32 v40, 0, v2
	v_add_f32_e32 v46, v56, v57
	v_add_f32_e32 v50, v52, v53
	v_mov_b32_e32 v41, v62
	v_mov_b32_e32 v43, v63
	v_mov_b32_e32 v47, v60
	v_mov_b32_e32 v51, v61
	v_pk_add_f32 v[40:41], v[40:41], v[42:43]
	v_pk_add_f32 v[42:43], v[46:47], v[50:51]
	s_andn2_b64 vcc, exec, s[8:9]
	v_pk_add_f32 v[40:41], v[40:41], v[42:43]
	s_mov_b64 s[12:13], -1
	v_add_f32_e32 v2, v40, v41
	ds_bpermute_b32 v40, v99, v2
	s_waitcnt lgkmcnt(0)
	v_add_f32_e32 v2, v2, v40
	ds_bpermute_b32 v40, v100, v2
	s_waitcnt lgkmcnt(0)
	v_add_f32_e32 v2, v2, v40
	ds_bpermute_b32 v40, v101, v2
	s_waitcnt lgkmcnt(0)
	v_add_f32_e32 v2, v2, v40
	ds_bpermute_b32 v40, v102, v2
	s_waitcnt lgkmcnt(0)
	v_add_f32_e32 v2, v2, v40
	ds_bpermute_b32 v40, v103, v2
	s_waitcnt lgkmcnt(0)
	v_add_f32_e32 v2, v2, v40
	ds_bpermute_b32 v40, v104, v2
	s_waitcnt lgkmcnt(0)
	v_add_f32_e32 v64, v2, v40
	v_fmamk_f32 v55, v64, 0xba800000, v55
	v_fmac_f32_e32 v54, 0xba800000, v64
	v_fmamk_f32 v59, v64, 0xba800000, v59
	v_fmac_f32_e32 v58, 0xba800000, v64
	v_pk_mul_f32 v[40:41], v[58:59], v[58:59]
	v_pk_mul_f32 v[42:43], v[54:55], v[54:55]
	v_fmamk_f32 v49, v64, 0xba800000, v49
	v_pk_mov_b32 v[46:47], v[42:43], v[40:41] op_sel:[1,0]
	v_mov_b32_e32 v43, v41
	v_fmac_f32_e32 v48, 0xba800000, v64
	v_fmamk_f32 v45, v64, 0xba800000, v45
	v_fmac_f32_e32 v44, 0xba800000, v64
	v_pk_add_f32 v[40:41], v[46:47], v[42:43]
	v_pk_mul_f32 v[42:43], v[44:45], v[44:45]
	v_pk_mul_f32 v[46:47], v[48:49], v[48:49]
	v_fmac_f32_e32 v56, 0xba800000, v64
	v_pk_mov_b32 v[50:51], v[46:47], v[42:43] op_sel:[1,0]
	v_mov_b32_e32 v47, v43
	v_fmamk_f32 v57, v64, 0xba800000, v57
	v_fmac_f32_e32 v52, 0xba800000, v64
	v_mul_f32_e32 v2, v56, v56
	v_pk_add_f32 v[42:43], v[50:51], v[46:47]
	v_fmamk_f32 v53, v64, 0xba800000, v53
	v_pk_fma_f32 v[46:47], v[56:57], v[56:57], v[2:3] op_sel_hi:[1,1,0]
	v_mul_f32_e32 v2, v52, v52
	v_pk_add_f32 v[40:41], v[40:41], v[40:41] op_sel_hi:[0,1]
	v_pk_add_f32 v[42:43], v[42:43], v[42:43] op_sel_hi:[0,1]
	v_pk_fma_f32 v[50:51], v[52:53], v[52:53], v[2:3] op_sel_hi:[1,1,0]
	v_fmamk_f32 v61, v64, 0xba800000, v61
	v_fmac_f32_e32 v60, 0xba800000, v64
	v_fmamk_f32 v63, v64, 0xba800000, v63
	v_fmac_f32_e32 v62, 0xba800000, v64
	v_mul_f32_e32 v46, v62, v62
	v_mul_f32_e32 v50, v63, v63
	v_mul_f32_e32 v40, v60, v60
	v_mul_f32_e32 v42, v61, v61
	v_pk_add_f32 v[46:47], v[46:47], v[50:51]
	v_pk_add_f32 v[40:41], v[40:41], v[42:43]
	s_nop 0
	v_pk_add_f32 v[40:41], v[46:47], v[40:41]
	s_nop 0
	v_add_f32_e32 v2, v40, v41
	ds_bpermute_b32 v40, v99, v2
	s_waitcnt lgkmcnt(0)
	v_add_f32_e32 v2, v2, v40
	ds_bpermute_b32 v40, v100, v2
	s_waitcnt lgkmcnt(0)
	v_add_f32_e32 v2, v2, v40
	ds_bpermute_b32 v40, v101, v2
	s_waitcnt lgkmcnt(0)
	v_add_f32_e32 v2, v2, v40
	ds_bpermute_b32 v40, v102, v2
	s_waitcnt lgkmcnt(0)
	v_add_f32_e32 v2, v2, v40
	ds_bpermute_b32 v40, v103, v2
	s_waitcnt lgkmcnt(0)
	v_add_f32_e32 v2, v2, v40
	ds_bpermute_b32 v40, v104, v2
	s_waitcnt lgkmcnt(0)
	v_add_f32_e32 v2, v2, v40
	v_fmamk_f32 v2, v2, 0x3a800000, v241
	v_rsq_f32_e32 v2, v2
	s_nop 0
	v_pk_mul_f32 v[48:49], v[48:49], v[2:3] op_sel_hi:[1,0]
	v_pk_mul_f32 v[44:45], v[44:45], v[2:3] op_sel_hi:[1,0]
	v_pk_mul_f32 v[40:41], v[54:55], v[2:3] op_sel_hi:[1,0]
	v_pk_mul_f32 v[42:43], v[58:59], v[2:3] op_sel_hi:[1,0]
	v_pk_fma_f32 v[46:47], v[14:15], v[44:45], v[30:31]
	v_pk_fma_f32 v[44:45], v[12:13], v[48:49], v[28:29]
	v_pk_mul_f32 v[48:49], v[56:57], v[2:3] op_sel_hi:[1,0]
	v_pk_mul_f32 v[50:51], v[52:53], v[2:3] op_sel_hi:[1,0]
	v_pk_mul_f32 v[52:53], v[62:63], v[2:3] op_sel_hi:[1,0]
	v_pk_mul_f32 v[54:55], v[60:61], v[2:3] op_sel_hi:[1,0]
	v_pk_fma_f32 v[42:43], v[18:19], v[42:43], v[34:35]
	v_pk_fma_f32 v[40:41], v[16:17], v[40:41], v[32:33]
	v_pk_fma_f32 v[50:51], v[10:11], v[50:51], v[26:27]
	v_pk_fma_f32 v[48:49], v[8:9], v[48:49], v[24:25]
	v_pk_fma_f32 v[54:55], v[6:7], v[54:55], v[22:23]
	v_pk_fma_f32 v[52:53], v[4:5], v[52:53], v[20:21]
	s_cbranch_vccnz .LBB0_1066
	v_cvt_pk_bf16_f32 v56, v40, v41
	v_cvt_pk_bf16_f32 v57, v42, v43
	v_cvt_pk_bf16_f32 v58, v44, v45
	v_cvt_pk_bf16_f32 v59, v46, v47
	v_cvt_pk_bf16_f32 v60, v48, v49
	v_cvt_pk_bf16_f32 v61, v50, v51
	v_cvt_pk_bf16_f32 v62, v52, v53
	v_cvt_pk_bf16_f32 v63, v54, v55
	global_store_dwordx4 v[88:89], v[56:59], off
	global_store_dwordx4 v[88:89], v[60:63], off offset:16
	s_lshl_b64 s[12:13], s[10:11], 10
	v_mov_b32_e32 v56, v3
	v_mov_b32_e32 v57, v3
	v_mov_b32_e32 v58, v3
	v_mov_b32_e32 v59, v3
	v_cvt_pk_fp8_f32 v56, v40, v41
	v_cvt_pk_fp8_f32 v57, v44, v45
	v_cvt_pk_fp8_f32 v58, v48, v49
	v_cvt_pk_fp8_f32 v59, v52, v53
	v_cvt_pk_fp8_f32 v56, v42, v43 op_sel:[0,0,1]
	v_cvt_pk_fp8_f32 v57, v46, v47 op_sel:[0,0,1]
	v_cvt_pk_fp8_f32 v58, v50, v51 op_sel:[0,0,1]
	v_cvt_pk_fp8_f32 v59, v54, v55 op_sel:[0,0,1]
	v_lshl_add_u64 v[60:61], v[84:85], 0, s[12:13]
	s_mov_b64 s[12:13], 0
	global_store_dwordx4 v[60:61], v[56:59], off
